# out-proj GEMM: first 8 residual x loads issued before the K-loop into loop-free registers; plus EpiUp store address chain simplification
# speedup vs baseline: 1.0001x; 1.0001x over previous
.LBB0_1430:
	v_and_b32_e32 v233, 3, v219
	s_add_u32 s92, s74, 0x19800000
	v_and_b32_e32 v232, 15, v0
	v_lshlrev_b32_e32 v2, 4, v233
	v_lshlrev_b32_e32 v4, 2, v0
	s_sext_i32_i8 s83, s4
	s_addc_u32 s93, s75, 0
	v_lshl_or_b32 v3, v232, 6, v2
	s_lshl_b32 s4, s5, 13
	v_and_b32_e32 v4, 32, v4
	v_bitop3_b32 v3, v3, s4, v4 bitop3:0xde
	s_lshl_b32 s4, s17, 5
	s_and_b32 s57, s4, 0x60
	v_lshlrev_b32_e32 v5, 6, v0
	s_movk_i32 s4, 0x3c0
	s_lshl_b32 s53, s5, 6
	v_and_or_b32 v2, v5, s4, v2
	s_lshl_b32 s4, s57, 7
	v_bitop3_b32 v2, s4, v2, v4 bitop3:0xf6
	s_add_u32 s4, s60, 0x80
	s_waitcnt vmcnt(2)
	s_barrier
	s_addc_u32 s5, s61, 0
	s_add_i32 s68, s28, 0x18000
	s_mov_b32 s17, m0
	s_mov_b32 m0, s68
	s_nop 2
	global_load_lds_dwordx4 v229, s[4:5]
	s_mov_b32 m0, s17
	s_add_i32 s69, s28, 0x1a000
	s_mov_b32 s17, m0
	s_mov_b32 m0, s69
	s_nop 2
	global_load_lds_dwordx4 v231, s[4:5]
	s_mov_b32 m0, s17
	s_add_u32 s4, s58, 0x80
	s_addc_u32 s5, s59, 0
	s_add_i32 s76, s28, 0x8000
	s_mov_b32 s17, m0
	s_mov_b32 m0, s76
	s_nop 2
	global_load_lds_dwordx4 v228, s[4:5]
	s_mov_b32 m0, s17
	s_add_i32 s77, s28, 0xa000
	s_mov_b32 s17, m0
	s_mov_b32 m0, s77
	s_nop 2
	global_load_lds_dwordx4 v230, s[4:5]
	s_mov_b32 m0, s17
	s_add_u32 s4, s60, 0x40080
	s_addc_u32 s5, s61, 0
	s_add_i32 s78, s28, 0x1c000
	s_mov_b32 s17, m0
	s_mov_b32 m0, s78
	s_nop 2
	global_load_lds_dwordx4 v229, s[4:5]
	s_mov_b32 m0, s17
	s_add_i32 s79, s28, 0x1e000
	s_mov_b32 s17, m0
	s_mov_b32 m0, s79
	s_nop 2
	global_load_lds_dwordx4 v231, s[4:5]
	s_mov_b32 m0, s17
	s_waitcnt vmcnt(6)
	s_add_i32 s80, s28, 0xc000
	s_cmpk_lt_u32 s16, 0x100
	v_add_u32_e32 v2, 0, v2
	s_cselect_b64 s[16:17], -1, 0
	s_add_i32 s81, s28, 0xe000
	s_ashr_i32 s82, s90, 31
	v_mov_b64_e32 v[220:221], 0x100
	v_mov_b64_e32 v[222:223], 0xff
	v_add_u32_e32 v234, 0x10000, v2
	v_add_u32_e32 v235, 0x14000, v2
	v_add_u32_e32 v236, 0, v3
	v_add_u32_e32 v237, 0x18000, v2
	v_add_u32_e32 v238, 0x1c000, v2
	v_mov_b32_e32 v225, 0
	s_lshl_b32 s2, s56, 8
	s_add_i32 s2, s2, s53
	v_add_lshl_u32 v224, s2, v232, 10
	s_lshl_b32 s2, s83, 8
	s_or_b32 s2, s2, s57
	v_lshlrev_b32_e32 v226, 3, v233
	v_readlane_b32 s0, v253, 8
	v_add3_u32 v224, s2, v226, v224
	v_readlane_b32 s1, v253, 9
	s_mov_b64 s[2:3], 0x10000
	s_nop 1
	v_lshl_add_u64 v[226:227], v[224:225], 2, s[0:1]
	global_load_dwordx4 v[240:243], v[226:227], off
	global_load_dwordx4 v[244:247], v[226:227], off offset:16
	global_load_dwordx4 v[210:213], v[226:227], off offset:528
	global_load_dwordx4 v[214:217], v[226:227], off offset:512
	v_lshl_add_u64 v[248:249], v[226:227], 0, s[2:3]
	global_load_dwordx4 v[206:209], v[248:249], off
	global_load_dwordx4 v[202:205], v[248:249], off offset:16
	global_load_dwordx4 v[198:201], v[248:249], off offset:512
	global_load_dwordx4 v[194:197], v[248:249], off offset:528
	s_mov_b32 s32, 1
	s_barrier
	s_branch .LBB0_1433

.LBB0_1443:
	v_mov_b32_e32 v130, v232
	v_mov_b32_e32 v131, v233
	s_lshl_b32 s19, s56, 8
	s_add_i32 s19, s19, s53
	v_add_lshl_u32 v130, s19, v130, 10
	s_lshl_b32 s19, s83, 8
	s_or_b32 s19, s19, s57
	v_lshlrev_b32_e32 v131, 3, v131
	v_readlane_b32 s0, v253, 8
	v_add3_u32 v224, s19, v131, v130
	v_readlane_b32 s1, v253, 9
	s_mov_b64 s[58:59], 0x10000
	s_mov_b32 s19, 0x20000
	v_lshl_add_u64 v[226:227], v[224:225], 2, s[0:1]
	s_cmp_lg_u32 s32, 0
	s_mov_b32 s32, 0
	s_cbranch_scc1 .Lxpf_have
	global_load_dwordx4 v[240:243], v[226:227], off
	global_load_dwordx4 v[244:247], v[226:227], off offset:16
	global_load_dwordx4 v[210:213], v[226:227], off offset:528
	global_load_dwordx4 v[214:217], v[226:227], off offset:512
	v_add_co_u32_e32 v132, vcc, s29, v226
	v_lshl_add_u64 v[130:131], v[226:227], 0, s[58:59]
	s_nop 0
	v_addc_co_u32_e32 v133, vcc, 0, v227, vcc
	global_load_dwordx4 v[206:209], v[132:133], off
	global_load_dwordx4 v[202:205], v[130:131], off offset:16
	s_mov_b64 s[58:59], 0x10200
	v_lshl_add_u64 v[130:131], v[226:227], 0, s[58:59]
	global_load_dwordx4 v[198:201], v[132:133], off offset:512
	global_load_dwordx4 v[194:197], v[130:131], off offset:16
.Lxpf_have:
	v_add_co_u32_e32 v132, vcc, s19, v226
	s_mov_b64 s[58:59], 0x20000
	s_nop 0
	v_addc_co_u32_e32 v133, vcc, 0, v227, vcc
	v_lshl_add_u64 v[130:131], v[226:227], 0, s[58:59]
	global_load_dwordx4 v[190:193], v[132:133], off
	global_load_dwordx4 v[186:189], v[130:131], off offset:16
	s_mov_b64 s[58:59], 0x20200
	s_mov_b32 s19, 0x30000
	v_lshl_add_u64 v[130:131], v[226:227], 0, s[58:59]
	global_load_dwordx4 v[182:185], v[132:133], off offset:512
	global_load_dwordx4 v[178:181], v[130:131], off offset:16
	s_mov_b64 s[58:59], 0x30000
	v_add_co_u32_e32 v132, vcc, s19, v226
	v_lshl_add_u64 v[130:131], v[226:227], 0, s[58:59]
	s_nop 0
	v_addc_co_u32_e32 v133, vcc, 0, v227, vcc
	s_mov_b64 s[58:59], 0x30200
	s_mov_b32 s19, 0x80000
	global_load_dwordx4 v[174:177], v[132:133], off
	global_load_dwordx4 v[170:173], v[130:131], off offset:16
	v_lshl_add_u64 v[130:131], v[226:227], 0, s[58:59]
	global_load_dwordx4 v[166:169], v[132:133], off offset:512
	global_load_dwordx4 v[162:165], v[130:131], off offset:16
	s_mov_b64 s[58:59], 0x80000
	v_add_co_u32_e32 v132, vcc, s19, v226
	v_lshl_add_u64 v[130:131], v[226:227], 0, s[58:59]
	s_nop 0
	v_addc_co_u32_e32 v133, vcc, 0, v227, vcc
	s_mov_b64 s[58:59], 0x80200
	s_mov_b32 s19, 0x90000
	global_load_dwordx4 v[158:161], v[132:133], off
	global_load_dwordx4 v[154:157], v[130:131], off offset:16
	v_lshl_add_u64 v[130:131], v[226:227], 0, s[58:59]
	global_load_dwordx4 v[150:153], v[132:133], off offset:512
	global_load_dwordx4 v[146:149], v[130:131], off offset:16
	s_mov_b64 s[58:59], 0x90000
	v_add_co_u32_e32 v132, vcc, s19, v226
	v_lshl_add_u64 v[130:131], v[226:227], 0, s[58:59]
	s_nop 0
	v_addc_co_u32_e32 v133, vcc, 0, v227, vcc
	s_mov_b64 s[58:59], 0x90200
	global_load_dwordx4 v[142:145], v[132:133], off
	global_load_dwordx4 v[138:141], v[130:131], off offset:16
	v_lshl_add_u64 v[130:131], v[226:227], 0, s[58:59]
	global_load_dwordx4 v[134:137], v[132:133], off offset:512
	s_nop 0
	global_load_dwordx4 v[130:133], v[130:131], off offset:16
	s_mov_b32 s19, 0x8000
	s_mov_b64 s[58:59], 0xa0000
	v_readlane_b32 s4, v253, 12
	v_readlane_b32 s5, v253, 13
	s_mov_b64 s[4:5], -1
	v_readlane_b32 s2, v253, 10
	v_readlane_b32 s3, v253, 11
	v_readlane_b32 s6, v253, 14
	v_readlane_b32 s7, v253, 15
	v_readlane_b32 s8, v253, 16
	v_readlane_b32 s9, v253, 17
	v_readlane_b32 s10, v253, 18
	v_readlane_b32 s11, v253, 19
	v_readlane_b32 s12, v253, 20
	v_readlane_b32 s13, v253, 21
	v_readlane_b32 s14, v253, 22
	v_readlane_b32 s15, v253, 23
	s_waitcnt vmcnt(23)
	v_pk_add_f32 v[128:129], v[128:129], v[242:243]
	v_pk_add_f32 v[126:127], v[126:127], v[240:241]
	s_waitcnt vmcnt(22)
	v_pk_add_f32 v[240:241], v[124:125], v[246:247]
	v_pk_add_f32 v[122:123], v[122:123], v[244:245]
	v_cvt_pk_bf16_f32 v124, v126, v127
	v_cvt_pk_bf16_f32 v125, v128, v129
	v_cvt_pk_bf16_f32 v126, v122, v123
	v_cvt_pk_bf16_f32 v127, v240, v241
	v_lshl_add_u64 v[122:123], v[224:225], 1, s[92:93]
	global_store_dwordx4 v[122:123], v[124:127], off
	s_waitcnt vmcnt(21)
	v_pk_add_f32 v[120:121], v[120:121], v[216:217]
	v_pk_add_f32 v[118:119], v[118:119], v[214:215]
	v_pk_add_f32 v[124:125], v[112:113], v[212:213]
	v_pk_add_f32 v[112:113], v[110:111], v[210:211]
	v_cvt_pk_bf16_f32 v110, v118, v119
	v_cvt_pk_bf16_f32 v111, v120, v121
	v_cvt_pk_bf16_f32 v112, v112, v113
	v_cvt_pk_bf16_f32 v113, v124, v125
	global_store_dwordx4 v[122:123], v[110:113], off offset:256
	s_waitcnt vmcnt(19)
	v_pk_add_f32 v[104:105], v[104:105], v[200:201]
	v_pk_add_f32 v[102:103], v[102:103], v[198:199]
	v_pk_add_f32 v[110:111], v[116:117], v[208:209]
	v_pk_add_f32 v[112:113], v[114:115], v[206:207]
	v_pk_add_f32 v[114:115], v[108:109], v[204:205]
	v_pk_add_f32 v[108:109], v[106:107], v[202:203]
	v_cvt_pk_bf16_f32 v107, v110, v111
	v_add_co_u32_e32 v110, vcc, s19, v122
	v_cvt_pk_bf16_f32 v106, v112, v113
	v_cvt_pk_bf16_f32 v108, v108, v109
	v_cvt_pk_bf16_f32 v109, v114, v115
	v_addc_co_u32_e32 v111, vcc, 0, v123, vcc
	global_store_dwordx4 v[110:111], v[106:109], off
	s_mov_b32 s19, 0xa0000
	s_waitcnt vmcnt(18)
	v_pk_add_f32 v[94:95], v[94:95], v[190:191]
	v_pk_add_f32 v[106:107], v[100:101], v[196:197]
	v_pk_add_f32 v[100:101], v[98:99], v[194:195]
	v_cvt_pk_bf16_f32 v98, v102, v103
	v_cvt_pk_bf16_f32 v99, v104, v105
	v_cvt_pk_bf16_f32 v100, v100, v101
	v_cvt_pk_bf16_f32 v101, v106, v107
	global_store_dwordx4 v[110:111], v[98:101], off offset:256
	v_pk_add_f32 v[96:97], v[96:97], v[192:193]
	s_waitcnt vmcnt(18)
	v_pk_add_f32 v[128:129], v[92:93], v[188:189]
	v_add_co_u32_e32 v100, vcc, s19, v226
	v_lshl_add_u64 v[98:99], v[226:227], 0, s[58:59]
	s_nop 0
	v_addc_co_u32_e32 v101, vcc, 0, v227, vcc
	global_load_dwordx4 v[106:109], v[100:101], off
	global_load_dwordx4 v[110:113], v[98:99], off offset:16
	s_mov_b64 s[58:59], 0xa0200
	s_mov_b32 s19, 0xb0000
	v_lshl_add_u64 v[98:99], v[226:227], 0, s[58:59]
	global_load_dwordx4 v[114:117], v[100:101], off offset:512
	global_load_dwordx4 v[118:121], v[98:99], off offset:16
	v_add_co_u32_e32 v100, vcc, s19, v226
	s_mov_b64 s[58:59], 0xb0000
	s_nop 0
	v_addc_co_u32_e32 v101, vcc, 0, v227, vcc
	v_lshl_add_u64 v[98:99], v[226:227], 0, s[58:59]
	global_load_dwordx4 v[124:127], v[100:101], off
	global_load_dwordx4 v[194:197], v[98:99], off offset:16
	s_mov_b64 s[58:59], 0xb0200
	v_lshl_add_u64 v[98:99], v[226:227], 0, s[58:59]
	global_load_dwordx4 v[102:105], v[100:101], off offset:512
	s_nop 0
	global_load_dwordx4 v[98:101], v[98:99], off offset:16
	v_pk_add_f32 v[92:93], v[90:91], v[186:187]
	v_cvt_pk_bf16_f32 v90, v94, v95
	v_add_co_u32_e32 v94, vcc, s29, v122
	v_cvt_pk_bf16_f32 v91, v96, v97
	v_cvt_pk_bf16_f32 v92, v92, v93
	v_cvt_pk_bf16_f32 v93, v128, v129
	v_addc_co_u32_e32 v95, vcc, 0, v123, vcc
	global_store_dwordx4 v[94:95], v[90:93], off
	s_waitcnt vmcnt(26)
	v_pk_add_f32 v[84:85], v[84:85], v[184:185]
	v_pk_add_f32 v[82:83], v[82:83], v[182:183]
	s_waitcnt vmcnt(25)
	v_pk_add_f32 v[90:91], v[76:77], v[180:181]
	v_pk_add_f32 v[76:77], v[74:75], v[178:179]
	v_cvt_pk_bf16_f32 v74, v82, v83
	v_cvt_pk_bf16_f32 v75, v84, v85
	v_cvt_pk_bf16_f32 v76, v76, v77
	v_cvt_pk_bf16_f32 v77, v90, v91
	global_store_dwordx4 v[94:95], v[74:77], off offset:256
	s_waitcnt vmcnt(24)
	v_pk_add_f32 v[78:79], v[78:79], v[170:171]
	s_mov_b32 s19, 0x18000
	v_pk_add_f32 v[76:77], v[88:89], v[176:177]
	v_pk_add_f32 v[74:75], v[86:87], v[174:175]
	v_pk_add_f32 v[80:81], v[80:81], v[172:173]
	v_cvt_pk_bf16_f32 v74, v74, v75
	v_cvt_pk_bf16_f32 v75, v76, v77
	v_cvt_pk_bf16_f32 v76, v78, v79
	v_add_co_u32_e32 v78, vcc, s19, v122
	v_cvt_pk_bf16_f32 v77, v80, v81
	s_nop 0
	v_addc_co_u32_e32 v79, vcc, 0, v123, vcc
	global_store_dwordx4 v[78:79], v[74:77], off
	s_waitcnt vmcnt(24)
	v_pk_add_f32 v[72:73], v[72:73], v[168:169]
	v_pk_add_f32 v[70:71], v[70:71], v[166:167]
	s_waitcnt vmcnt(23)
	v_pk_add_f32 v[74:75], v[68:69], v[164:165]
	v_pk_add_f32 v[68:69], v[66:67], v[162:163]
	v_cvt_pk_bf16_f32 v66, v70, v71
	v_cvt_pk_bf16_f32 v67, v72, v73
	v_cvt_pk_bf16_f32 v68, v68, v69
	v_cvt_pk_bf16_f32 v69, v74, v75
	s_waitcnt vmcnt(22)
	v_pk_add_f32 v[62:63], v[62:63], v[158:159]
	s_mov_b32 s19, 0x40000
	global_store_dwordx4 v[78:79], v[66:69], off offset:256
	v_pk_add_f32 v[64:65], v[64:65], v[160:161]
	s_waitcnt vmcnt(21)
	v_pk_add_f32 v[52:53], v[52:53], v[152:153]
	v_pk_add_f32 v[66:67], v[60:61], v[156:157]
	v_pk_add_f32 v[60:61], v[58:59], v[154:155]
	v_cvt_pk_bf16_f32 v58, v62, v63
	v_add_co_u32_e32 v62, vcc, s19, v122
	v_cvt_pk_bf16_f32 v59, v64, v65
	v_cvt_pk_bf16_f32 v60, v60, v61
	v_cvt_pk_bf16_f32 v61, v66, v67
	v_addc_co_u32_e32 v63, vcc, 0, v123, vcc
	global_store_dwordx4 v[62:63], v[58:61], off
	v_pk_add_f32 v[50:51], v[50:51], v[150:151]
	s_waitcnt vmcnt(19)
	v_pk_add_f32 v[46:47], v[46:47], v[138:139]
	v_pk_add_f32 v[58:59], v[44:45], v[148:149]
	v_pk_add_f32 v[44:45], v[42:43], v[146:147]
	v_cvt_pk_bf16_f32 v42, v50, v51
	v_cvt_pk_bf16_f32 v43, v52, v53
	v_cvt_pk_bf16_f32 v44, v44, v45
	v_cvt_pk_bf16_f32 v45, v58, v59
	global_store_dwordx4 v[62:63], v[42:45], off offset:256
	s_mov_b32 s19, 0x48000
	v_pk_add_f32 v[48:49], v[48:49], v[140:141]
	v_pk_add_f32 v[44:45], v[56:57], v[144:145]
	v_pk_add_f32 v[42:43], v[54:55], v[142:143]
	s_waitcnt vmcnt(19)
	v_pk_add_f32 v[36:37], v[36:37], v[136:137]
	v_cvt_pk_bf16_f32 v42, v42, v43
	v_cvt_pk_bf16_f32 v43, v44, v45
	v_cvt_pk_bf16_f32 v44, v46, v47
	v_add_co_u32_e32 v46, vcc, s19, v122
	v_cvt_pk_bf16_f32 v45, v48, v49
	s_nop 0
	v_addc_co_u32_e32 v47, vcc, 0, v123, vcc
	global_store_dwordx4 v[46:47], v[42:45], off
	v_pk_add_f32 v[34:35], v[34:35], v[134:135]
	s_waitcnt vmcnt(13)
	v_pk_add_f32 v[30:31], v[30:31], v[110:111]
	v_pk_add_f32 v[42:43], v[28:29], v[132:133]
	v_pk_add_f32 v[28:29], v[26:27], v[130:131]
	v_cvt_pk_bf16_f32 v26, v34, v35
	v_cvt_pk_bf16_f32 v27, v36, v37
	v_cvt_pk_bf16_f32 v28, v28, v29
	v_cvt_pk_bf16_f32 v29, v42, v43
	global_store_dwordx4 v[46:47], v[26:29], off offset:256
	s_mov_b32 s19, 0x50000
	v_pk_add_f32 v[32:33], v[32:33], v[112:113]
	v_pk_add_f32 v[28:29], v[40:41], v[108:109]
	v_pk_add_f32 v[26:27], v[38:39], v[106:107]
	s_waitcnt vmcnt(13)
	v_pk_add_f32 v[20:21], v[20:21], v[116:117]
	v_cvt_pk_bf16_f32 v26, v26, v27
	v_cvt_pk_bf16_f32 v27, v28, v29
	v_cvt_pk_bf16_f32 v28, v30, v31
	v_add_co_u32_e32 v30, vcc, s19, v122
	v_cvt_pk_bf16_f32 v29, v32, v33
	s_nop 0
	v_addc_co_u32_e32 v31, vcc, 0, v123, vcc
	global_store_dwordx4 v[30:31], v[26:29], off
	v_pk_add_f32 v[18:19], v[18:19], v[114:115]
	s_waitcnt vmcnt(11)
	v_pk_add_f32 v[14:15], v[14:15], v[194:195]
	v_pk_add_f32 v[26:27], v[12:13], v[120:121]
	v_pk_add_f32 v[12:13], v[10:11], v[118:119]
	v_cvt_pk_bf16_f32 v10, v18, v19
	v_cvt_pk_bf16_f32 v11, v20, v21
	v_cvt_pk_bf16_f32 v12, v12, v13
	v_cvt_pk_bf16_f32 v13, v26, v27
	global_store_dwordx4 v[30:31], v[10:13], off offset:256
	s_mov_b32 s19, 0x58000
	v_pk_add_f32 v[16:17], v[16:17], v[196:197]
	v_pk_add_f32 v[12:13], v[24:25], v[126:127]
	v_pk_add_f32 v[10:11], v[22:23], v[124:125]
	s_waitcnt vmcnt(11)
	v_pk_add_f32 v[8:9], v[8:9], v[104:105]
	v_cvt_pk_bf16_f32 v10, v10, v11
	v_cvt_pk_bf16_f32 v11, v12, v13
	v_cvt_pk_bf16_f32 v12, v14, v15
	v_add_co_u32_e32 v14, vcc, s19, v122
	v_cvt_pk_bf16_f32 v13, v16, v17
	s_nop 0
	v_addc_co_u32_e32 v15, vcc, 0, v123, vcc
	global_store_dwordx4 v[14:15], v[10:13], off
	v_pk_add_f32 v[6:7], v[6:7], v[102:103]
	s_andn2_b64 vcc, exec, s[40:41]
	s_waitcnt vmcnt(11)
	v_pk_add_f32 v[10:11], v[4:5], v[100:101]
	v_pk_add_f32 v[4:5], v[2:3], v[98:99]
	v_cvt_pk_bf16_f32 v2, v6, v7
	v_cvt_pk_bf16_f32 v3, v8, v9
	v_cvt_pk_bf16_f32 v4, v4, v5
	v_cvt_pk_bf16_f32 v5, v10, v11
	global_store_dwordx4 v[14:15], v[2:5], off offset:256
	s_cbranch_vccnz .LBB0_1432
	s_andn2_b64 vcc, exec, s[94:95]
	s_cbranch_vccnz .LBB0_1431
	s_barrier
	s_branch .LBB0_1431

.LBB0_1916:
	s_mov_b32 s29, 0
	s_nop 15
	s_nop 15
	v_mov_b32_e32 v4, v166
	v_mov_b32_e32 v2, v167
	v_mov_b32_e32 v3, s24
	s_add_u32 s40, s2, 0xffffff00
	ds_read_b32 v3, v3 offset:288
	s_addc_u32 s41, s23, -1
	s_lshl_b32 s2, s31, 11
	s_add_i32 s2, s2, 0
	v_lshl_add_u32 v18, v2, 3, s83
	s_add_i32 s2, s2, 0x21000
	v_lshl_add_u32 v5, v18, 3, s2
	ds_read_b128 v[14:17], v5
	s_waitcnt lgkmcnt(1)
	v_readfirstlane_b32 s8, v3
	s_lshl_b32 s8, s8, 2
	s_add_i32 s8, s8, 0
	s_add_i32 s8, s8, 0x201c0
	v_mov_b32_e32 v2, s8
	ds_read2_b32 v[2:3], v2 offset1:32
	v_add_u32_e32 v19, s82, v4
	ds_read_b128 v[10:13], v5 offset:16
	ds_read_b128 v[6:9], v5 offset:32
	v_add_u32_e32 v22, 16, v19
	v_add_u32_e32 v24, 32, v19
	s_waitcnt lgkmcnt(2)
	v_readfirstlane_b32 s9, v2
	v_lshl_add_u32 v2, v19, 2, s2
	ds_read_b32 v20, v2 offset:1024
	v_readfirstlane_b32 s8, v3
	s_sub_i32 s8, s36, s8
	v_lshl_add_u32 v23, v22, 2, s2
	v_lshl_add_u32 v25, v24, 2, s2
	s_lshl_b32 s8, s8, 8
	ds_read_b128 v[2:5], v5 offset:48
	ds_read_b32 v23, v23 offset:1024
	ds_read_b32 v25, v25 offset:1024
	v_add_u32_e32 v21, s8, v19
	s_waitcnt lgkmcnt(3)
	v_mul_f32_e32 v20, 0x3b800000, v20
	v_cmp_gt_i32_e32 vcc, s9, v21
	s_waitcnt lgkmcnt(1)
	v_mul_f32_e32 v21, 0x3b800000, v23
	v_add_u32_e32 v26, 0xa0, v19
	v_cndmask_b32_e32 v180, 0, v20, vcc
	v_add_u32_e32 v20, s8, v22
	v_cmp_gt_i32_e32 vcc, s9, v20
	v_add_u32_e32 v20, s8, v24
	v_add_u32_e32 v22, 0x80, v19
	v_cndmask_b32_e32 v164, 0, v21, vcc
	s_waitcnt lgkmcnt(0)
	v_mul_f32_e32 v21, 0x3b800000, v25
	v_cmp_gt_i32_e32 vcc, s9, v20
	v_add_u32_e32 v20, 48, v19
	v_add_u32_e32 v24, 0x90, v19
	v_cndmask_b32_e32 v162, 0, v21, vcc
	v_lshl_add_u32 v21, v20, 2, s2
	v_lshl_add_u32 v23, v22, 2, s2
	v_lshl_add_u32 v25, v24, 2, s2
	v_lshl_add_u32 v27, v26, 2, s2
	v_add_u32_e32 v29, 0xb0, v19
	v_add_u32_e32 v20, s8, v20
	v_lshl_add_u32 v28, v29, 2, s2
	ds_read_b32 v21, v21 offset:1024
	ds_read_b32 v23, v23 offset:1024
	ds_read_b32 v25, v25 offset:1024
	ds_read_b32 v27, v27 offset:1024
	ds_read_b32 v31, v28 offset:1024
	s_waitcnt lgkmcnt(4)
	v_mul_f32_e32 v21, 0x3b800000, v21
	v_cmp_gt_i32_e32 vcc, s9, v20
	v_add_u32_e32 v20, s8, v22
	s_lshl_b32 s42, s14, 7
	v_cndmask_b32_e32 v32, 0, v21, vcc
	s_waitcnt lgkmcnt(3)
	v_mul_f32_e32 v21, 0x3b800000, v23
	v_cmp_gt_i32_e32 vcc, s9, v20
	v_add_u32_e32 v20, s8, v24
	v_mov_b32_e32 v24, v14
	v_cndmask_b32_e32 v30, 0, v21, vcc
	s_waitcnt lgkmcnt(2)
	v_mul_f32_e32 v21, 0x3b800000, v25
	v_mov_b32_e32 v25, v16
	v_pk_fma_f32 v[182:183], v[158:159], v[180:181], v[24:25] op_sel_hi:[1,0,1]
	v_mov_b32_e32 v16, v15
	v_min_f32_e32 v182, 0x40e00000, v182
	v_min_f32_e32 v183, 0x40e00000, v183
	v_pk_mul_f32 v[184:185], v[182:183], s[20:21] op_sel_hi:[1,0]
	v_cmp_gt_i32_e32 vcc, s9, v20
	v_exp_f32_e32 v184, v184
	v_exp_f32_e32 v185, v185
	v_add_u32_e32 v20, s8, v26
	v_cndmask_b32_e32 v28, 0, v21, vcc
	s_waitcnt lgkmcnt(1)
	v_mul_f32_e32 v21, 0x3b800000, v27
	v_pk_add_f32 v[14:15], v[184:185], 1.0 op_sel_hi:[1,0]
	v_pk_fma_f32 v[184:185], v[126:127], v[180:181], v[16:17] op_sel_hi:[1,0,1]
	v_rcp_f32_e32 v14, v14
	v_rcp_f32_e32 v15, v15
	v_med3_f32 v184, v184, s37, v176
	v_med3_f32 v185, v185, s37, v176
	v_cmp_gt_i32_e32 vcc, s9, v20
	v_pk_mul_f32 v[14:15], v[182:183], v[14:15]
	v_add_u32_e32 v20, s8, v29
	v_pk_fma_f32 v[182:183], v[184:185], v[14:15], v[14:15]
	v_mov_b32_e32 v14, v10
	v_mov_b32_e32 v15, v12
	v_pk_fma_f32 v[184:185], v[160:161], v[180:181], v[14:15] op_sel_hi:[1,0,1]
	v_mov_b32_e32 v12, v11
	v_min_f32_e32 v184, 0x40e00000, v184
	v_min_f32_e32 v185, 0x40e00000, v185
	v_pk_mul_f32 v[186:187], v[184:185], s[20:21] op_sel_hi:[1,0]
	v_cndmask_b32_e32 v26, 0, v21, vcc
	v_exp_f32_e32 v186, v186
	v_exp_f32_e32 v187, v187
	s_waitcnt lgkmcnt(0)
	v_mul_f32_e32 v21, 0x3b800000, v31
	v_cmp_gt_i32_e32 vcc, s9, v20
	v_pk_add_f32 v[10:11], v[186:187], 1.0 op_sel_hi:[1,0]
	v_cndmask_b32_e32 v22, 0, v21, vcc
	v_rcp_f32_e32 v10, v10
	v_rcp_f32_e32 v11, v11
	v_cvt_pk_fp8_f32 v21, v182, v183
	v_pk_fma_f32 v[182:183], v[128:129], v[180:181], v[12:13] op_sel_hi:[1,0,1]
	v_pk_mul_f32 v[10:11], v[184:185], v[10:11]
	v_med3_f32 v182, v182, s37, v176
	v_med3_f32 v183, v183, s37, v176
	v_pk_fma_f32 v[182:183], v[182:183], v[10:11], v[10:11]
	v_mov_b32_e32 v10, v6
	v_mov_b32_e32 v11, v8
	v_pk_fma_f32 v[184:185], v[154:155], v[180:181], v[10:11] op_sel_hi:[1,0,1]
	v_mov_b32_e32 v8, v7
	v_min_f32_e32 v184, 0x40e00000, v184
	v_min_f32_e32 v185, 0x40e00000, v185
	v_pk_mul_f32 v[186:187], v[184:185], s[20:21] op_sel_hi:[1,0]
	v_cvt_pk_fp8_f32 v21, v182, v183 op_sel:[0,0,1]
	v_exp_f32_e32 v186, v186
	v_exp_f32_e32 v187, v187
	v_pk_fma_f32 v[182:183], v[122:123], v[180:181], v[8:9] op_sel_hi:[1,0,1]
	v_med3_f32 v182, v182, s37, v176
	v_pk_add_f32 v[6:7], v[186:187], 1.0 op_sel_hi:[1,0]
	v_med3_f32 v183, v183, s37, v176
	v_rcp_f32_e32 v6, v6
	v_rcp_f32_e32 v7, v7
	v_lshl_add_u32 v20, s36, 8, v19
	s_ashr_i32 s43, s42, 31
	v_pk_mul_f32 v[6:7], v[184:185], v[6:7]
	v_ashrrev_i32_e32 v19, 31, v18
	v_pk_fma_f32 v[182:183], v[182:183], v[6:7], v[6:7]
	v_mov_b32_e32 v6, v2
	v_mov_b32_e32 v7, v4
	v_pk_fma_f32 v[184:185], v[156:157], v[180:181], v[6:7] op_sel_hi:[1,0,1]
	v_mov_b32_e32 v4, v3
	v_min_f32_e32 v184, 0x40e00000, v184
	v_min_f32_e32 v185, 0x40e00000, v185
	v_pk_mul_f32 v[186:187], v[184:185], s[20:21] op_sel_hi:[1,0]
	v_pk_fma_f32 v[180:181], v[124:125], v[180:181], v[4:5] op_sel_hi:[1,0,1]
	v_exp_f32_e32 v186, v186
	v_exp_f32_e32 v187, v187
	v_cvt_pk_fp8_f32 v27, v182, v183
	v_med3_f32 v180, v180, s37, v176
	v_med3_f32 v181, v181, s37, v176
	v_pk_add_f32 v[2:3], v[186:187], 1.0 op_sel_hi:[1,0]
	v_pk_fma_f32 v[182:183], v[150:151], v[164:165], v[24:25] op_sel_hi:[1,0,1]
	v_rcp_f32_e32 v2, v2
	v_rcp_f32_e32 v3, v3
	v_min_f32_e32 v182, 0x40e00000, v182
	v_min_f32_e32 v183, 0x40e00000, v183
	s_and_b64 vcc, exec, s[6:7]
	v_pk_mul_f32 v[2:3], v[184:185], v[2:3]
	v_pk_mul_f32 v[184:185], v[182:183], s[20:21] op_sel_hi:[1,0]
	v_pk_fma_f32 v[2:3], v[180:181], v[2:3], v[2:3]
	v_exp_f32_e32 v184, v184
	v_cvt_pk_fp8_f32 v27, v2, v3 op_sel:[0,0,1]
	v_mov_b32_e32 v2, v21
	v_ashrrev_i32_e32 v21, 31, v20
	v_lshlrev_b64 v[180:181], 10, v[20:21]
	v_exp_f32_e32 v185, v185
	v_lshl_add_u64 v[180:181], s[12:13], 0, v[180:181]
	v_mov_b32_e32 v3, v27
	v_lshl_add_u64 v[180:181], v[180:181], 0, s[42:43]
	v_lshl_add_u64 v[188:189], v[180:181], 0, v[18:19]
	global_store_dwordx2 v[188:189], v[2:3], off
	v_pk_add_f32 v[2:3], v[184:185], 1.0 op_sel_hi:[1,0]
	v_pk_fma_f32 v[180:181], v[118:119], v[164:165], v[16:17] op_sel_hi:[1,0,1]
	v_rcp_f32_e32 v2, v2
	v_rcp_f32_e32 v3, v3
	v_med3_f32 v180, v180, s37, v176
	v_med3_f32 v181, v181, s37, v176
	v_pk_mul_f32 v[2:3], v[182:183], v[2:3]
	v_pk_fma_f32 v[182:183], v[152:153], v[164:165], v[14:15] op_sel_hi:[1,0,1]
	v_pk_fma_f32 v[2:3], v[180:181], v[2:3], v[2:3]
	v_min_f32_e32 v182, 0x40e00000, v182
	v_min_f32_e32 v183, 0x40e00000, v183
	v_pk_mul_f32 v[184:185], v[182:183], s[20:21] op_sel_hi:[1,0]
	v_cvt_pk_fp8_f32 v21, v2, v3
	v_exp_f32_e32 v184, v184
	v_exp_f32_e32 v185, v185
	v_pk_fma_f32 v[180:181], v[120:121], v[164:165], v[12:13] op_sel_hi:[1,0,1]
	v_med3_f32 v180, v180, s37, v176
	v_pk_add_f32 v[2:3], v[184:185], 1.0 op_sel_hi:[1,0]
	v_med3_f32 v181, v181, s37, v176
	v_rcp_f32_e32 v2, v2
	v_rcp_f32_e32 v3, v3
	s_nop 0
	v_pk_mul_f32 v[2:3], v[182:183], v[2:3]
	v_pk_fma_f32 v[182:183], v[146:147], v[164:165], v[10:11] op_sel_hi:[1,0,1]
	v_pk_fma_f32 v[2:3], v[180:181], v[2:3], v[2:3]
	v_min_f32_e32 v182, 0x40e00000, v182
	v_min_f32_e32 v183, 0x40e00000, v183
	v_pk_mul_f32 v[184:185], v[182:183], s[20:21] op_sel_hi:[1,0]
	v_cvt_pk_fp8_f32 v21, v2, v3 op_sel:[0,0,1]
	v_exp_f32_e32 v184, v184
	v_exp_f32_e32 v185, v185
	v_pk_fma_f32 v[180:181], v[114:115], v[164:165], v[8:9] op_sel_hi:[1,0,1]
	v_pk_add_f32 v[2:3], v[184:185], 1.0 op_sel_hi:[1,0]
	s_nop 0
	v_rcp_f32_e32 v2, v2
	v_rcp_f32_e32 v3, v3
	v_med3_f32 v180, v180, s37, v176
	v_med3_f32 v181, v181, s37, v176
	v_pk_mul_f32 v[2:3], v[182:183], v[2:3]
	v_pk_fma_f32 v[182:183], v[148:149], v[164:165], v[6:7] op_sel_hi:[1,0,1]
	v_pk_fma_f32 v[2:3], v[180:181], v[2:3], v[2:3]
	v_min_f32_e32 v182, 0x40e00000, v182
	v_min_f32_e32 v183, 0x40e00000, v183
	v_pk_mul_f32 v[184:185], v[182:183], s[20:21] op_sel_hi:[1,0]
	v_cvt_pk_fp8_f32 v27, v2, v3
	v_exp_f32_e32 v184, v184
	v_exp_f32_e32 v185, v185
	v_pk_fma_f32 v[180:181], v[116:117], v[164:165], v[4:5] op_sel_hi:[1,0,1]
	v_pk_add_f32 v[2:3], v[184:185], 1.0 op_sel_hi:[1,0]
	s_nop 0
	v_rcp_f32_e32 v2, v2
	v_rcp_f32_e32 v3, v3
	v_med3_f32 v180, v180, s37, v176
	v_med3_f32 v181, v181, s37, v176
	v_pk_mul_f32 v[2:3], v[182:183], v[2:3]
	v_pk_fma_f32 v[182:183], v[142:143], v[162:163], v[24:25] op_sel_hi:[1,0,1]
	v_pk_fma_f32 v[2:3], v[180:181], v[2:3], v[2:3]
	v_min_f32_e32 v182, 0x40e00000, v182
	v_min_f32_e32 v183, 0x40e00000, v183
	v_cvt_pk_fp8_f32 v27, v2, v3 op_sel:[0,0,1]
	v_pk_mul_f32 v[184:185], v[182:183], s[20:21] op_sel_hi:[1,0]
	v_exp_f32_e32 v184, v184
	v_exp_f32_e32 v185, v185
	v_mov_b32_e32 v2, v21
	v_mov_b32_e32 v3, v27
	s_mov_b32 s28, 0x4000
	v_lshl_add_u64 v[180:181], v[188:189], 0, s[28:29]
	global_store_dwordx2 v[180:181], v[2:3], off
	v_pk_add_f32 v[2:3], v[184:185], 1.0 op_sel_hi:[1,0]
	v_pk_fma_f32 v[180:181], v[110:111], v[162:163], v[16:17] op_sel_hi:[1,0,1]
	v_rcp_f32_e32 v2, v2
	v_rcp_f32_e32 v3, v3
	v_med3_f32 v180, v180, s37, v176
	v_med3_f32 v181, v181, s37, v176
	v_pk_mul_f32 v[2:3], v[182:183], v[2:3]
	v_pk_fma_f32 v[182:183], v[144:145], v[162:163], v[14:15] op_sel_hi:[1,0,1]
	v_pk_fma_f32 v[2:3], v[180:181], v[2:3], v[2:3]
	v_min_f32_e32 v182, 0x40e00000, v182
	v_min_f32_e32 v183, 0x40e00000, v183
	v_pk_mul_f32 v[184:185], v[182:183], s[20:21] op_sel_hi:[1,0]
	v_cvt_pk_fp8_f32 v21, v2, v3
	v_exp_f32_e32 v184, v184
	v_exp_f32_e32 v185, v185
	v_pk_fma_f32 v[180:181], v[112:113], v[162:163], v[12:13] op_sel_hi:[1,0,1]
	v_med3_f32 v180, v180, s37, v176
	v_pk_add_f32 v[2:3], v[184:185], 1.0 op_sel_hi:[1,0]
	v_med3_f32 v181, v181, s37, v176
	v_rcp_f32_e32 v2, v2
	v_rcp_f32_e32 v3, v3
	s_nop 0
	v_pk_mul_f32 v[2:3], v[182:183], v[2:3]
	v_pk_fma_f32 v[182:183], v[138:139], v[162:163], v[10:11] op_sel_hi:[1,0,1]
	v_pk_fma_f32 v[2:3], v[180:181], v[2:3], v[2:3]
	v_min_f32_e32 v182, 0x40e00000, v182
	v_min_f32_e32 v183, 0x40e00000, v183
	v_pk_mul_f32 v[184:185], v[182:183], s[20:21] op_sel_hi:[1,0]
	v_cvt_pk_fp8_f32 v21, v2, v3 op_sel:[0,0,1]
	v_exp_f32_e32 v184, v184
	v_exp_f32_e32 v185, v185
	v_pk_fma_f32 v[180:181], v[106:107], v[162:163], v[8:9] op_sel_hi:[1,0,1]
	v_pk_add_f32 v[2:3], v[184:185], 1.0 op_sel_hi:[1,0]
	s_nop 0
	v_rcp_f32_e32 v2, v2
	v_rcp_f32_e32 v3, v3
	v_med3_f32 v180, v180, s37, v176
	v_med3_f32 v181, v181, s37, v176
	v_pk_mul_f32 v[2:3], v[182:183], v[2:3]
	v_pk_fma_f32 v[182:183], v[140:141], v[162:163], v[6:7] op_sel_hi:[1,0,1]
	v_pk_fma_f32 v[2:3], v[180:181], v[2:3], v[2:3]
	v_min_f32_e32 v182, 0x40e00000, v182
	v_min_f32_e32 v183, 0x40e00000, v183
	v_pk_mul_f32 v[184:185], v[182:183], s[20:21] op_sel_hi:[1,0]
	v_cvt_pk_fp8_f32 v27, v2, v3
	v_exp_f32_e32 v184, v184
	v_exp_f32_e32 v185, v185
	v_pk_fma_f32 v[180:181], v[108:109], v[162:163], v[4:5] op_sel_hi:[1,0,1]
	v_pk_add_f32 v[2:3], v[184:185], 1.0 op_sel_hi:[1,0]
	s_nop 0
	v_rcp_f32_e32 v2, v2
	v_rcp_f32_e32 v3, v3
	v_med3_f32 v180, v180, s37, v176
	v_med3_f32 v181, v181, s37, v176
	v_pk_mul_f32 v[2:3], v[182:183], v[2:3]
	v_pk_fma_f32 v[182:183], v[134:135], v[32:33], v[24:25] op_sel_hi:[1,0,1]
	v_pk_fma_f32 v[2:3], v[180:181], v[2:3], v[2:3]
	v_min_f32_e32 v182, 0x40e00000, v182
	v_min_f32_e32 v183, 0x40e00000, v183
	v_cvt_pk_fp8_f32 v27, v2, v3 op_sel:[0,0,1]
	v_pk_mul_f32 v[184:185], v[182:183], s[20:21] op_sel_hi:[1,0]
	v_exp_f32_e32 v184, v184
	v_exp_f32_e32 v185, v185
	v_mov_b32_e32 v2, v21
	v_mov_b32_e32 v3, v27
	s_mov_b32 s28, 0x8000
	v_lshl_add_u64 v[180:181], v[188:189], 0, s[28:29]
	global_store_dwordx2 v[180:181], v[2:3], off
	v_pk_add_f32 v[2:3], v[184:185], 1.0 op_sel_hi:[1,0]
	v_pk_fma_f32 v[180:181], v[102:103], v[32:33], v[16:17] op_sel_hi:[1,0,1]
	v_rcp_f32_e32 v2, v2
	v_rcp_f32_e32 v3, v3
	v_med3_f32 v180, v180, s37, v176
	v_med3_f32 v181, v181, s37, v176
	v_pk_mul_f32 v[2:3], v[182:183], v[2:3]
	v_pk_fma_f32 v[182:183], v[136:137], v[32:33], v[14:15] op_sel_hi:[1,0,1]
	v_pk_fma_f32 v[2:3], v[180:181], v[2:3], v[2:3]
	v_min_f32_e32 v182, 0x40e00000, v182
	v_min_f32_e32 v183, 0x40e00000, v183
	v_pk_mul_f32 v[184:185], v[182:183], s[20:21] op_sel_hi:[1,0]
	v_cvt_pk_fp8_f32 v21, v2, v3
	v_exp_f32_e32 v184, v184
	v_exp_f32_e32 v185, v185
	v_pk_fma_f32 v[180:181], v[104:105], v[32:33], v[12:13] op_sel_hi:[1,0,1]
	v_med3_f32 v180, v180, s37, v176
	v_pk_add_f32 v[2:3], v[184:185], 1.0 op_sel_hi:[1,0]
	v_med3_f32 v181, v181, s37, v176
	v_rcp_f32_e32 v2, v2
	v_rcp_f32_e32 v3, v3
	s_nop 0
	v_pk_mul_f32 v[2:3], v[182:183], v[2:3]
	v_pk_fma_f32 v[182:183], v[130:131], v[32:33], v[10:11] op_sel_hi:[1,0,1]
	v_pk_fma_f32 v[2:3], v[180:181], v[2:3], v[2:3]
	v_min_f32_e32 v182, 0x40e00000, v182
	v_min_f32_e32 v183, 0x40e00000, v183
	v_pk_mul_f32 v[184:185], v[182:183], s[20:21] op_sel_hi:[1,0]
	v_cvt_pk_fp8_f32 v21, v2, v3 op_sel:[0,0,1]
	v_exp_f32_e32 v184, v184
	v_exp_f32_e32 v185, v185
	v_pk_fma_f32 v[180:181], v[98:99], v[32:33], v[8:9] op_sel_hi:[1,0,1]
	v_pk_add_f32 v[2:3], v[184:185], 1.0 op_sel_hi:[1,0]
	s_nop 0
	v_rcp_f32_e32 v2, v2
	v_rcp_f32_e32 v3, v3
	v_med3_f32 v180, v180, s37, v176
	v_med3_f32 v181, v181, s37, v176
	v_pk_mul_f32 v[2:3], v[182:183], v[2:3]
	v_pk_fma_f32 v[182:183], v[132:133], v[32:33], v[6:7] op_sel_hi:[1,0,1]
	v_pk_fma_f32 v[2:3], v[180:181], v[2:3], v[2:3]
	v_min_f32_e32 v182, 0x40e00000, v182
	v_min_f32_e32 v183, 0x40e00000, v183
	v_pk_mul_f32 v[184:185], v[182:183], s[20:21] op_sel_hi:[1,0]
	v_cvt_pk_fp8_f32 v27, v2, v3
	v_exp_f32_e32 v184, v184
	v_exp_f32_e32 v185, v185
	v_pk_fma_f32 v[32:33], v[100:101], v[32:33], v[4:5] op_sel_hi:[1,0,1]
	v_pk_fma_f32 v[180:181], v[94:95], v[30:31], v[24:25] op_sel_hi:[1,0,1]
	v_med3_f32 v32, v32, s37, v176
	v_pk_add_f32 v[2:3], v[184:185], 1.0 op_sel_hi:[1,0]
	v_med3_f32 v33, v33, s37, v176
	v_rcp_f32_e32 v2, v2
	v_rcp_f32_e32 v3, v3
	v_min_f32_e32 v180, 0x40e00000, v180
	v_min_f32_e32 v181, 0x40e00000, v181
	v_pk_mul_f32 v[2:3], v[182:183], v[2:3]
	s_nop 0
	v_pk_fma_f32 v[2:3], v[32:33], v[2:3], v[2:3]
	v_cvt_pk_fp8_f32 v27, v2, v3 op_sel:[0,0,1]
	v_pk_mul_f32 v[182:183], v[180:181], s[20:21] op_sel_hi:[1,0]
	v_exp_f32_e32 v182, v182
	v_exp_f32_e32 v183, v183
	v_mov_b32_e32 v2, v21
	v_mov_b32_e32 v3, v27
	s_mov_b32 s28, 0xc000
	v_lshl_add_u64 v[32:33], v[188:189], 0, s[28:29]
	global_store_dwordx2 v[32:33], v[2:3], off
	v_pk_add_f32 v[32:33], v[182:183], 1.0 op_sel_hi:[1,0]
	v_pk_fma_f32 v[182:183], v[62:63], v[30:31], v[16:17] op_sel_hi:[1,0,1]
	v_rcp_f32_e32 v32, v32
	v_rcp_f32_e32 v33, v33
	v_med3_f32 v182, v182, s37, v176
	v_med3_f32 v183, v183, s37, v176
	v_pk_mul_f32 v[32:33], v[180:181], v[32:33]
	v_pk_fma_f32 v[180:181], v[96:97], v[30:31], v[14:15] op_sel_hi:[1,0,1]
	v_pk_fma_f32 v[32:33], v[182:183], v[32:33], v[32:33]
	v_min_f32_e32 v180, 0x40e00000, v180
	v_min_f32_e32 v181, 0x40e00000, v181
	v_pk_mul_f32 v[184:185], v[180:181], s[20:21] op_sel_hi:[1,0]
	v_cvt_pk_fp8_f32 v3, v32, v33
	v_exp_f32_e32 v184, v184
	v_exp_f32_e32 v185, v185
	v_pk_fma_f32 v[182:183], v[64:65], v[30:31], v[12:13] op_sel_hi:[1,0,1]
	v_med3_f32 v182, v182, s37, v176
	v_pk_add_f32 v[32:33], v[184:185], 1.0 op_sel_hi:[1,0]
	v_med3_f32 v183, v183, s37, v176
	v_rcp_f32_e32 v32, v32
	v_rcp_f32_e32 v33, v33
	s_nop 0
	v_pk_mul_f32 v[32:33], v[180:181], v[32:33]
	v_pk_fma_f32 v[180:181], v[90:91], v[30:31], v[10:11] op_sel_hi:[1,0,1]
	v_pk_fma_f32 v[32:33], v[182:183], v[32:33], v[32:33]
	v_min_f32_e32 v180, 0x40e00000, v180
	v_min_f32_e32 v181, 0x40e00000, v181
	v_pk_mul_f32 v[184:185], v[180:181], s[20:21] op_sel_hi:[1,0]
	v_cvt_pk_fp8_f32 v3, v32, v33 op_sel:[0,0,1]
	v_exp_f32_e32 v184, v184
	v_exp_f32_e32 v185, v185
	v_pk_fma_f32 v[182:183], v[58:59], v[30:31], v[8:9] op_sel_hi:[1,0,1]
	v_med3_f32 v182, v182, s37, v176
	v_pk_add_f32 v[32:33], v[184:185], 1.0 op_sel_hi:[1,0]
	v_med3_f32 v183, v183, s37, v176
	v_rcp_f32_e32 v32, v32
	v_rcp_f32_e32 v33, v33
	s_nop 0
	v_pk_mul_f32 v[32:33], v[180:181], v[32:33]
	v_pk_fma_f32 v[180:181], v[92:93], v[30:31], v[6:7] op_sel_hi:[1,0,1]
	v_pk_fma_f32 v[32:33], v[182:183], v[32:33], v[32:33]
	v_min_f32_e32 v180, 0x40e00000, v180
	v_min_f32_e32 v181, 0x40e00000, v181
	v_pk_mul_f32 v[184:185], v[180:181], s[20:21] op_sel_hi:[1,0]
	v_cvt_pk_fp8_f32 v23, v32, v33
	v_exp_f32_e32 v184, v184
	v_exp_f32_e32 v185, v185
	v_pk_fma_f32 v[30:31], v[60:61], v[30:31], v[4:5] op_sel_hi:[1,0,1]
	v_med3_f32 v30, v30, s37, v176
	v_pk_add_f32 v[32:33], v[184:185], 1.0 op_sel_hi:[1,0]
	v_med3_f32 v31, v31, s37, v176
	v_rcp_f32_e32 v32, v32
	v_rcp_f32_e32 v33, v33
	s_nop 0
	v_pk_mul_f32 v[32:33], v[180:181], v[32:33]
	s_nop 0
	v_pk_fma_f32 v[30:31], v[30:31], v[32:33], v[32:33]
	v_pk_fma_f32 v[32:33], v[86:87], v[28:29], v[24:25] op_sel_hi:[1,0,1]
	v_cvt_pk_fp8_f32 v23, v30, v31 op_sel:[0,0,1]
	v_min_f32_e32 v32, 0x40e00000, v32
	v_min_f32_e32 v33, 0x40e00000, v33
	v_mov_b32_e32 v30, v3
	v_pk_mul_f32 v[180:181], v[32:33], s[20:21] op_sel_hi:[1,0]
	v_exp_f32_e32 v180, v180
	v_exp_f32_e32 v181, v181
	v_mov_b32_e32 v31, v23
	s_mov_b32 s28, 0x20000
	v_lshl_add_u64 v[2:3], v[188:189], 0, s[28:29]
	global_store_dwordx2 v[2:3], v[30:31], off
	v_pk_add_f32 v[2:3], v[180:181], 1.0 op_sel_hi:[1,0]
	v_pk_fma_f32 v[30:31], v[54:55], v[28:29], v[16:17] op_sel_hi:[1,0,1]
	v_rcp_f32_e32 v2, v2
	v_rcp_f32_e32 v3, v3
	v_med3_f32 v30, v30, s37, v176
	v_med3_f32 v31, v31, s37, v176
	v_pk_mul_f32 v[2:3], v[32:33], v[2:3]
	v_pk_fma_f32 v[32:33], v[88:89], v[28:29], v[14:15] op_sel_hi:[1,0,1]
	v_pk_fma_f32 v[2:3], v[30:31], v[2:3], v[2:3]
	v_min_f32_e32 v32, 0x40e00000, v32
	v_min_f32_e32 v33, 0x40e00000, v33
	v_pk_mul_f32 v[180:181], v[32:33], s[20:21] op_sel_hi:[1,0]
	v_cvt_pk_fp8_f32 v21, v2, v3
	v_exp_f32_e32 v180, v180
	v_exp_f32_e32 v181, v181
	v_pk_fma_f32 v[30:31], v[56:57], v[28:29], v[12:13] op_sel_hi:[1,0,1]
	v_med3_f32 v30, v30, s37, v176
	v_pk_add_f32 v[2:3], v[180:181], 1.0 op_sel_hi:[1,0]
	v_med3_f32 v31, v31, s37, v176
	v_rcp_f32_e32 v2, v2
	v_rcp_f32_e32 v3, v3
	s_nop 0
	v_pk_mul_f32 v[2:3], v[32:33], v[2:3]
	v_pk_fma_f32 v[32:33], v[82:83], v[28:29], v[10:11] op_sel_hi:[1,0,1]
	v_pk_fma_f32 v[2:3], v[30:31], v[2:3], v[2:3]
	v_min_f32_e32 v32, 0x40e00000, v32
	v_min_f32_e32 v33, 0x40e00000, v33
	v_pk_mul_f32 v[180:181], v[32:33], s[20:21] op_sel_hi:[1,0]
	v_cvt_pk_fp8_f32 v21, v2, v3 op_sel:[0,0,1]
	v_exp_f32_e32 v180, v180
	v_exp_f32_e32 v181, v181
	v_pk_fma_f32 v[30:31], v[50:51], v[28:29], v[8:9] op_sel_hi:[1,0,1]
	v_pk_add_f32 v[2:3], v[180:181], 1.0 op_sel_hi:[1,0]
	s_nop 0
	v_rcp_f32_e32 v2, v2
	v_rcp_f32_e32 v3, v3
	v_med3_f32 v30, v30, s37, v176
	v_med3_f32 v31, v31, s37, v176
	v_pk_mul_f32 v[2:3], v[32:33], v[2:3]
	v_pk_fma_f32 v[32:33], v[84:85], v[28:29], v[6:7] op_sel_hi:[1,0,1]
	v_pk_fma_f32 v[2:3], v[30:31], v[2:3], v[2:3]
	v_min_f32_e32 v32, 0x40e00000, v32
	v_min_f32_e32 v33, 0x40e00000, v33
	v_pk_mul_f32 v[180:181], v[32:33], s[20:21] op_sel_hi:[1,0]
	v_cvt_pk_fp8_f32 v27, v2, v3
	v_exp_f32_e32 v180, v180
	v_exp_f32_e32 v181, v181
	v_pk_fma_f32 v[28:29], v[52:53], v[28:29], v[4:5] op_sel_hi:[1,0,1]
	v_pk_fma_f32 v[30:31], v[78:79], v[26:27], v[24:25] op_sel_hi:[1,0,1]
	v_med3_f32 v28, v28, s37, v176
	v_pk_add_f32 v[2:3], v[180:181], 1.0 op_sel_hi:[1,0]
	v_med3_f32 v29, v29, s37, v176
	v_rcp_f32_e32 v2, v2
	v_rcp_f32_e32 v3, v3
	v_min_f32_e32 v30, 0x40e00000, v30
	v_min_f32_e32 v31, 0x40e00000, v31
	v_pk_mul_f32 v[2:3], v[32:33], v[2:3]
	s_nop 0
	v_pk_fma_f32 v[2:3], v[28:29], v[2:3], v[2:3]
	v_cvt_pk_fp8_f32 v27, v2, v3 op_sel:[0,0,1]
	s_nop 0
	v_mov_b32_e32 v3, v27
	v_pk_mul_f32 v[32:33], v[30:31], s[20:21] op_sel_hi:[1,0]
	v_mov_b32_e32 v2, v21
	v_exp_f32_e32 v32, v32
	v_exp_f32_e32 v33, v33
	s_mov_b32 s28, 0x24000
	v_lshl_add_u64 v[28:29], v[188:189], 0, s[28:29]
	global_store_dwordx2 v[28:29], v[2:3], off
	v_pk_add_f32 v[2:3], v[32:33], 1.0 op_sel_hi:[1,0]
	v_pk_fma_f32 v[28:29], v[46:47], v[26:27], v[16:17] op_sel_hi:[1,0,1]
	v_rcp_f32_e32 v2, v2
	v_rcp_f32_e32 v3, v3
	v_med3_f32 v28, v28, s37, v176
	v_med3_f32 v29, v29, s37, v176
	v_pk_mul_f32 v[2:3], v[30:31], v[2:3]
	v_pk_fma_f32 v[30:31], v[80:81], v[26:27], v[14:15] op_sel_hi:[1,0,1]
	v_pk_fma_f32 v[2:3], v[28:29], v[2:3], v[2:3]
	v_min_f32_e32 v30, 0x40e00000, v30
	v_min_f32_e32 v31, 0x40e00000, v31
	v_pk_mul_f32 v[32:33], v[30:31], s[20:21] op_sel_hi:[1,0]
	v_cvt_pk_fp8_f32 v21, v2, v3
	v_exp_f32_e32 v32, v32
	v_exp_f32_e32 v33, v33
	v_pk_fma_f32 v[28:29], v[48:49], v[26:27], v[12:13] op_sel_hi:[1,0,1]
	v_med3_f32 v28, v28, s37, v176
	v_pk_add_f32 v[2:3], v[32:33], 1.0 op_sel_hi:[1,0]
	v_med3_f32 v29, v29, s37, v176
	v_rcp_f32_e32 v2, v2
	v_rcp_f32_e32 v3, v3
	s_nop 0
	v_pk_mul_f32 v[2:3], v[30:31], v[2:3]
	v_pk_fma_f32 v[30:31], v[74:75], v[26:27], v[10:11] op_sel_hi:[1,0,1]
	v_pk_fma_f32 v[2:3], v[28:29], v[2:3], v[2:3]
	v_min_f32_e32 v30, 0x40e00000, v30
	v_min_f32_e32 v31, 0x40e00000, v31
	v_pk_mul_f32 v[32:33], v[30:31], s[20:21] op_sel_hi:[1,0]
	v_cvt_pk_fp8_f32 v21, v2, v3 op_sel:[0,0,1]
	v_exp_f32_e32 v32, v32
	v_exp_f32_e32 v33, v33
	v_pk_fma_f32 v[28:29], v[42:43], v[26:27], v[8:9] op_sel_hi:[1,0,1]
	v_pk_fma_f32 v[24:25], v[70:71], v[22:23], v[24:25] op_sel_hi:[1,0,1]
	v_med3_f32 v28, v28, s37, v176
	v_pk_add_f32 v[2:3], v[32:33], 1.0 op_sel_hi:[1,0]
	v_med3_f32 v29, v29, s37, v176
	v_rcp_f32_e32 v2, v2
	v_rcp_f32_e32 v3, v3
	v_min_f32_e32 v24, 0x40e00000, v24
	v_min_f32_e32 v25, 0x40e00000, v25
	v_pk_fma_f32 v[14:15], v[72:73], v[22:23], v[14:15] op_sel_hi:[1,0,1]
	v_pk_mul_f32 v[2:3], v[30:31], v[2:3]
	v_pk_fma_f32 v[30:31], v[76:77], v[26:27], v[6:7] op_sel_hi:[1,0,1]
	v_pk_fma_f32 v[2:3], v[28:29], v[2:3], v[2:3]
	v_min_f32_e32 v30, 0x40e00000, v30
	v_min_f32_e32 v31, 0x40e00000, v31
	v_pk_mul_f32 v[32:33], v[30:31], s[20:21] op_sel_hi:[1,0]
	v_exp_f32_e32 v32, v32
	v_exp_f32_e32 v33, v33
	v_cvt_pk_fp8_f32 v28, v2, v3
	v_pk_fma_f32 v[26:27], v[44:45], v[26:27], v[4:5] op_sel_hi:[1,0,1]
	v_min_f32_e32 v14, 0x40e00000, v14
	v_pk_add_f32 v[2:3], v[32:33], 1.0 op_sel_hi:[1,0]
	v_med3_f32 v26, v26, s37, v176
	v_rcp_f32_e32 v2, v2
	v_rcp_f32_e32 v3, v3
	v_med3_f32 v27, v27, s37, v176
	v_min_f32_e32 v15, 0x40e00000, v15
	v_pk_fma_f32 v[16:17], v[38:39], v[22:23], v[16:17] op_sel_hi:[1,0,1]
	v_pk_mul_f32 v[2:3], v[30:31], v[2:3]
	v_med3_f32 v16, v16, s37, v176
	v_pk_fma_f32 v[2:3], v[26:27], v[2:3], v[2:3]
	v_cvt_pk_fp8_f32 v28, v2, v3 op_sel:[0,0,1]
	s_nop 0
	v_mov_b32_e32 v3, v28
	v_pk_mul_f32 v[28:29], v[24:25], s[20:21] op_sel_hi:[1,0]
	v_mov_b32_e32 v2, v21
	v_exp_f32_e32 v28, v28
	v_exp_f32_e32 v29, v29
	s_mov_b32 s28, 0x28000
	v_lshl_add_u64 v[26:27], v[188:189], 0, s[28:29]
	global_store_dwordx2 v[26:27], v[2:3], off
	v_pk_add_f32 v[2:3], v[28:29], 1.0 op_sel_hi:[1,0]
	v_med3_f32 v17, v17, s37, v176
	v_rcp_f32_e32 v2, v2
	v_rcp_f32_e32 v3, v3
	v_pk_fma_f32 v[10:11], v[66:67], v[22:23], v[10:11] op_sel_hi:[1,0,1]
	v_pk_fma_f32 v[12:13], v[40:41], v[22:23], v[12:13] op_sel_hi:[1,0,1]
	v_min_f32_e32 v10, 0x40e00000, v10
	v_pk_mul_f32 v[2:3], v[24:25], v[2:3]
	v_pk_mul_f32 v[24:25], v[14:15], s[20:21] op_sel_hi:[1,0]
	v_pk_fma_f32 v[2:3], v[16:17], v[2:3], v[2:3]
	v_exp_f32_e32 v24, v24
	v_exp_f32_e32 v25, v25
	v_cvt_pk_fp8_f32 v16, v2, v3
	v_min_f32_e32 v11, 0x40e00000, v11
	v_pk_add_f32 v[2:3], v[24:25], 1.0 op_sel_hi:[1,0]
	v_med3_f32 v12, v12, s37, v176
	v_rcp_f32_e32 v2, v2
	v_rcp_f32_e32 v3, v3
	v_med3_f32 v13, v13, s37, v176
	v_pk_fma_f32 v[6:7], v[68:69], v[22:23], v[6:7] op_sel_hi:[1,0,1]
	v_pk_fma_f32 v[8:9], v[34:35], v[22:23], v[8:9] op_sel_hi:[1,0,1]
	v_pk_mul_f32 v[2:3], v[14:15], v[2:3]
	v_pk_mul_f32 v[14:15], v[10:11], s[20:21] op_sel_hi:[1,0]
	v_pk_fma_f32 v[2:3], v[12:13], v[2:3], v[2:3]
	v_exp_f32_e32 v14, v14
	v_exp_f32_e32 v15, v15
	v_cvt_pk_fp8_f32 v16, v2, v3 op_sel:[0,0,1]
	v_min_f32_e32 v6, 0x40e00000, v6
	v_pk_add_f32 v[2:3], v[14:15], 1.0 op_sel_hi:[1,0]
	v_min_f32_e32 v7, 0x40e00000, v7
	v_rcp_f32_e32 v2, v2
	v_rcp_f32_e32 v3, v3
	v_med3_f32 v8, v8, s37, v176
	v_med3_f32 v9, v9, s37, v176
	v_pk_fma_f32 v[4:5], v[36:37], v[22:23], v[4:5] op_sel_hi:[1,0,1]
	v_pk_mul_f32 v[2:3], v[10:11], v[2:3]
	v_pk_mul_f32 v[10:11], v[6:7], s[20:21] op_sel_hi:[1,0]
	v_pk_fma_f32 v[2:3], v[8:9], v[2:3], v[2:3]
	v_exp_f32_e32 v10, v10
	v_exp_f32_e32 v11, v11
	v_cvt_pk_fp8_f32 v8, v2, v3
	v_med3_f32 v4, v4, s37, v176
	v_pk_add_f32 v[2:3], v[10:11], 1.0 op_sel_hi:[1,0]
	v_med3_f32 v5, v5, s37, v176
	v_rcp_f32_e32 v2, v2
	v_rcp_f32_e32 v3, v3
	s_nop 0
	v_pk_mul_f32 v[2:3], v[6:7], v[2:3]
	s_nop 0
	v_pk_fma_f32 v[2:3], v[4:5], v[2:3], v[2:3]
	v_cvt_pk_fp8_f32 v8, v2, v3 op_sel:[0,0,1]
	s_nop 0
	v_mov_b32_e32 v3, v8
	v_mov_b32_e32 v2, v16
	s_mov_b32 s28, 0x2c000
	v_lshl_add_u64 v[4:5], v[188:189], 0, s[28:29]
	global_store_dwordx2 v[4:5], v[2:3], off
	s_cbranch_vccnz .LBB0_1920
	s_andn2_b64 vcc, exec, s[0:1]
	s_cbranch_vccnz .LBB0_1919
	s_barrier
